# attn_fast: the five 4-trip LDS-DMA staging loops (q, k, key state, v, value state) unrolled: no exec-mask loop branches between the prologue loads
# baseline (speedup 1.0000x reference)
_Z9attn_fastPKtS0_S0_S0_S0_S0_S0_S0_S0_PKfS2_Pt:
	s_load_dwordx8 s[36:43], s[0:1], 0x40
	v_and_b32_e32 v152, 63, v0
	v_bfe_u32 v153, v0, 6, 2
	v_mul_u32_u24_e32 v153, 0x1800, v153
	v_lshl_add_u32 v154, v152, 2, v153
	v_lshl_add_u32 v155, v152, 3, v153
	v_lshl_add_u32 v152, v152, 4, v153
	v_mov_b32_e32 v153, v155
	s_load_dwordx8 s[24:31], s[0:1], 0x0
	s_load_dwordx8 s[4:11], s[0:1], 0x20
	v_lshrrev_b32_e32 v2, 5, v0
	s_ashr_i32 s3, s2, 31
	v_bitop3_b32 v3, v2, v0, 31 bitop3:0x78
	v_lshlrev_b32_e32 v3, 4, v3
	v_lshlrev_b32_e32 v70, 4, v0
	s_lshl_b64 s[34:35], s[2:3], 15
	v_lshlrev_b32_e32 v2, 9, v2
	v_or_b32_e32 v6, 0xfffffe00, v0
	v_add_u32_e32 v7, 0, v70
	v_or3_b32 v2, s34, v2, v3
	v_mov_b32_e32 v3, s35
	v_mov_b32_e32 v1, v0
	v_add_u32_e32 v8, 0x18000, v7
	s_waitcnt lgkmcnt(0)
	v_lshl_add_u64 v[4:5], s[24:25], 0, v[2:3]
	s_mov_b64 s[0:1], 0
	s_mov_b64 s[12:13], 0x2000
	s_movk_i32 s14, 0x5ff
	v_mov_b32_e32 v9, v6
	v_readfirstlane_b32 s15, v8
	s_mov_b32 m0, s15
	v_add_u32_e32 v9, 0x200, v9
	global_load_lds_dwordx4 v[4:5], off
	v_cmp_lt_u32_e32 vcc, s14, v9
	v_add_u32_e32 v8, 0x2000, v8
	s_or_b64 s[0:1], vcc, s[0:1]
	v_lshl_add_u64 v[4:5], v[4:5], 0, s[12:13]
	v_readfirstlane_b32 s15, v8
	s_mov_b32 m0, s15
	v_add_u32_e32 v9, 0x200, v9
	global_load_lds_dwordx4 v[4:5], off
	v_cmp_lt_u32_e32 vcc, s14, v9
	v_add_u32_e32 v8, 0x2000, v8
	s_or_b64 s[0:1], vcc, s[0:1]
	v_lshl_add_u64 v[4:5], v[4:5], 0, s[12:13]
	v_readfirstlane_b32 s15, v8
	s_mov_b32 m0, s15
	v_add_u32_e32 v9, 0x200, v9
	global_load_lds_dwordx4 v[4:5], off
	v_cmp_lt_u32_e32 vcc, s14, v9
	v_add_u32_e32 v8, 0x2000, v8
	s_or_b64 s[0:1], vcc, s[0:1]
	v_lshl_add_u64 v[4:5], v[4:5], 0, s[12:13]
	v_readfirstlane_b32 s15, v8
	s_mov_b32 m0, s15
	v_add_u32_e32 v9, 0x200, v9
	global_load_lds_dwordx4 v[4:5], off
	v_cmp_lt_u32_e32 vcc, s14, v9
	v_add_u32_e32 v8, 0x2000, v8
	s_or_b64 s[0:1], vcc, s[0:1]
	v_lshl_add_u64 v[4:5], v[4:5], 0, s[12:13]
	s_or_b64 exec, exec, s[0:1]
	v_lshl_add_u64 v[4:5], s[26:27], 0, v[2:3]
	s_mov_b64 s[0:1], 0
	s_mov_b64 s[12:13], 0x2000
	s_movk_i32 s14, 0x5ff
	v_mov_b32_e32 v8, v6
	v_readfirstlane_b32 s15, v7
	s_mov_b32 m0, s15
	v_add_u32_e32 v8, 0x200, v8
	global_load_lds_dwordx4 v[4:5], off
	v_cmp_lt_u32_e32 vcc, s14, v8
	v_add_u32_e32 v7, 0x2000, v7
	s_or_b64 s[0:1], vcc, s[0:1]
	v_lshl_add_u64 v[4:5], v[4:5], 0, s[12:13]
	v_readfirstlane_b32 s15, v7
	s_mov_b32 m0, s15
	v_add_u32_e32 v8, 0x200, v8
	global_load_lds_dwordx4 v[4:5], off
	v_cmp_lt_u32_e32 vcc, s14, v8
	v_add_u32_e32 v7, 0x2000, v7
	s_or_b64 s[0:1], vcc, s[0:1]
	v_lshl_add_u64 v[4:5], v[4:5], 0, s[12:13]
	v_readfirstlane_b32 s15, v7
	s_mov_b32 m0, s15
	v_add_u32_e32 v8, 0x200, v8
	global_load_lds_dwordx4 v[4:5], off
	v_cmp_lt_u32_e32 vcc, s14, v8
	v_add_u32_e32 v7, 0x2000, v7
	s_or_b64 s[0:1], vcc, s[0:1]
	v_lshl_add_u64 v[4:5], v[4:5], 0, s[12:13]
	v_readfirstlane_b32 s15, v7
	s_mov_b32 m0, s15
	v_add_u32_e32 v8, 0x200, v8
	global_load_lds_dwordx4 v[4:5], off
	v_cmp_lt_u32_e32 vcc, s14, v8
	v_add_u32_e32 v7, 0x2000, v7
	s_or_b64 s[0:1], vcc, s[0:1]
	v_lshl_add_u64 v[4:5], v[4:5], 0, s[12:13]
	s_or_b64 exec, exec, s[0:1]
	v_add_u32_e32 v4, 0, v70
	v_add_u32_e32 v4, 0x8000, v4
	v_lshl_add_u64 v[2:3], s[10:11], 0, v[2:3]
	s_mov_b64 s[0:1], 0
	s_mov_b64 s[10:11], 0x2000
	s_movk_i32 s12, 0x5ff
	v_readfirstlane_b32 s13, v4
	s_mov_b32 m0, s13
	v_add_u32_e32 v6, 0x200, v6
	global_load_lds_dwordx4 v[2:3], off
	v_cmp_lt_u32_e32 vcc, s12, v6
	v_add_u32_e32 v4, 0x2000, v4
	s_or_b64 s[0:1], vcc, s[0:1]
	v_lshl_add_u64 v[2:3], v[2:3], 0, s[10:11]
	v_readfirstlane_b32 s13, v4
	s_mov_b32 m0, s13
	v_add_u32_e32 v6, 0x200, v6
	global_load_lds_dwordx4 v[2:3], off
	v_cmp_lt_u32_e32 vcc, s12, v6
	v_add_u32_e32 v4, 0x2000, v4
	s_or_b64 s[0:1], vcc, s[0:1]
	v_lshl_add_u64 v[2:3], v[2:3], 0, s[10:11]
	v_readfirstlane_b32 s13, v4
	s_mov_b32 m0, s13
	v_add_u32_e32 v6, 0x200, v6
	global_load_lds_dwordx4 v[2:3], off
	v_cmp_lt_u32_e32 vcc, s12, v6
	v_add_u32_e32 v4, 0x2000, v4
	s_or_b64 s[0:1], vcc, s[0:1]
	v_lshl_add_u64 v[2:3], v[2:3], 0, s[10:11]
	v_readfirstlane_b32 s13, v4
	s_mov_b32 m0, s13
	v_add_u32_e32 v6, 0x200, v6
	global_load_lds_dwordx4 v[2:3], off
	v_cmp_lt_u32_e32 vcc, s12, v6
	v_add_u32_e32 v4, 0x2000, v4
	s_or_b64 s[0:1], vcc, s[0:1]
	v_lshl_add_u64 v[2:3], v[2:3], 0, s[10:11]
	s_or_b64 exec, exec, s[0:1]
	s_movk_i32 s0, 0x200
	s_lshl_b64 s[10:11], s[2:3], 12
	v_cmp_gt_u32_e32 vcc, s0, v0
	s_and_saveexec_b64 s[0:1], vcc
	s_cbranch_execnz .LBB12_19
	s_or_b64 exec, exec, s[0:1]
	v_cmp_gt_u32_e64 s[0:1], 32, v0
	s_and_saveexec_b64 s[4:5], s[0:1]
	s_cbranch_execnz .LBB12_20

.LBB12_10:
	s_or_b64 exec, exec, s[4:5]
	v_lshlrev_b32_e32 v2, 4, v0
	v_and_b32_e32 v2, 0x1f80, v2
	v_mov_b32_e32 v3, 0
	v_lshl_add_u64 v[66:67], s[34:35], 0, v[2:3]
	v_lshl_add_u64 v[4:5], s[28:29], 0, v[66:67]
	s_mov_b64 s[4:5], 0
	s_movk_i32 s12, 0x70
	s_add_i32 s3, 0, 0x10000
	s_mov_b64 s[6:7], 0x2000
	s_movk_i32 s13, 0x5ff
	v_mov_b32_e32 v6, v70
	v_mov_b32_e32 v7, v1
	v_add_u32_e32 v10, s3, v6
	v_bitop3_b32 v2, v6, s12, v7 bitop3:0x48
	v_readfirstlane_b32 s0, v10
	v_lshl_add_u64 v[8:9], v[4:5], 0, v[2:3]
	s_mov_b32 m0, s0
	v_add_u32_e32 v2, 0x200, v7
	global_load_lds_dwordx4 v[8:9], off
	v_cmp_lt_u32_e64 s[0:1], s13, v7
	v_add_u32_e32 v6, 0x2000, v6
	v_lshl_add_u64 v[4:5], v[4:5], 0, s[6:7]
	s_or_b64 s[4:5], s[0:1], s[4:5]
	v_mov_b32_e32 v7, v2
	v_add_u32_e32 v10, s3, v6
	v_bitop3_b32 v2, v6, s12, v7 bitop3:0x48
	v_readfirstlane_b32 s0, v10
	v_lshl_add_u64 v[8:9], v[4:5], 0, v[2:3]
	s_mov_b32 m0, s0
	v_add_u32_e32 v2, 0x200, v7
	global_load_lds_dwordx4 v[8:9], off
	v_cmp_lt_u32_e64 s[0:1], s13, v7
	v_add_u32_e32 v6, 0x2000, v6
	v_lshl_add_u64 v[4:5], v[4:5], 0, s[6:7]
	s_or_b64 s[4:5], s[0:1], s[4:5]
	v_mov_b32_e32 v7, v2
	v_add_u32_e32 v10, s3, v6
	v_bitop3_b32 v2, v6, s12, v7 bitop3:0x48
	v_readfirstlane_b32 s0, v10
	v_lshl_add_u64 v[8:9], v[4:5], 0, v[2:3]
	s_mov_b32 m0, s0
	v_add_u32_e32 v2, 0x200, v7
	global_load_lds_dwordx4 v[8:9], off
	v_cmp_lt_u32_e64 s[0:1], s13, v7
	v_add_u32_e32 v6, 0x2000, v6
	v_lshl_add_u64 v[4:5], v[4:5], 0, s[6:7]
	s_or_b64 s[4:5], s[0:1], s[4:5]
	v_mov_b32_e32 v7, v2
	v_add_u32_e32 v10, s3, v6
	v_bitop3_b32 v2, v6, s12, v7 bitop3:0x48
	v_readfirstlane_b32 s0, v10
	v_lshl_add_u64 v[8:9], v[4:5], 0, v[2:3]
	s_mov_b32 m0, s0
	v_add_u32_e32 v2, 0x200, v7
	global_load_lds_dwordx4 v[8:9], off
	v_cmp_lt_u32_e64 s[0:1], s13, v7
	v_add_u32_e32 v6, 0x2000, v6
	v_lshl_add_u64 v[4:5], v[4:5], 0, s[6:7]
	s_or_b64 s[4:5], s[0:1], s[4:5]
	v_mov_b32_e32 v7, v2
	s_or_b64 exec, exec, s[4:5]
	s_and_saveexec_b64 s[0:1], vcc
	s_cbranch_execz .LBB12_14
	s_add_i32 s4, 0, 0x24000
	v_add_u32_e32 v6, s4, v70
	s_lshl_b64 s[4:5], s[10:11], 1
	s_add_u32 s4, s8, s4
	s_addc_u32 s5, s9, s5
	v_and_b32_e32 v2, 0x1f80, v70
	v_mov_b32_e32 v3, 0
	v_lshl_add_u64 v[4:5], s[4:5], 0, v[2:3]
	s_movk_i32 s4, 0x70
	v_bitop3_b32 v2, v70, s4, v0 bitop3:0x48
	v_readfirstlane_b32 s4, v6
	v_lshl_add_u64 v[2:3], v[4:5], 0, v[2:3]
	s_mov_b32 m0, s4
	s_nop 0
	global_load_lds_dwordx4 v[2:3], off
.LBB12_14:
	s_or_b64 exec, exec, s[0:1]
	v_lshrrev_b32_e32 v105, 2, v0
	v_and_b32_e32 v103, 15, v0
	v_lshrrev_b32_e32 v2, 4, v0
	v_bfe_u32 v104, v0, 4, 2
	v_and_or_b32 v102, v105, 48, v103
	s_add_i32 s33, 0, 0x18000
	v_bitop3_b32 v2, v2, v103, 3 bitop3:0x6c
	v_lshl_add_u32 v3, v102, 9, s33
	v_lshlrev_b32_e32 v78, 4, v2
	v_bitop3_b32 v4, v104, v103, 4 bitop3:0x36
	v_add_u32_e32 v2, v3, v78
	v_lshlrev_b32_e32 v77, 4, v4
	s_waitcnt vmcnt(5)
	s_barrier
	v_add_u32_e32 v4, v3, v77
	ds_read_b128 v[62:65], v2
	ds_read_b128 v[58:61], v4
	v_bitop3_b32 v2, v104, v103, 8 bitop3:0x36
	v_lshlrev_b32_e32 v76, 4, v2
	v_bitop3_b32 v4, v104, v103, 12 bitop3:0x36
	v_add_u32_e32 v2, v3, v76
	v_lshlrev_b32_e32 v75, 4, v4
	v_add_u32_e32 v4, v3, v75
	ds_read_b128 v[54:57], v2
	ds_read_b128 v[50:53], v4
	v_bitop3_b32 v2, v104, v103, 16 bitop3:0x36
	v_lshlrev_b32_e32 v74, 4, v2
	v_bitop3_b32 v4, v104, v103, 20 bitop3:0x36
	v_add_u32_e32 v2, v3, v74
	v_lshlrev_b32_e32 v72, 4, v4
	v_add_u32_e32 v4, v3, v72
	ds_read_b128 v[46:49], v2
	ds_read_b128 v[42:45], v4
	v_bitop3_b32 v2, v104, v103, 24 bitop3:0x36
	v_lshlrev_b32_e32 v73, 4, v2
	v_bitop3_b32 v4, v104, v103, 28 bitop3:0x36
	v_add_u32_e32 v2, v3, v73
	v_lshlrev_b32_e32 v71, 4, v4
	v_add_u32_e32 v3, v3, v71
	ds_read_b128 v[38:41], v2
	ds_read_b128 v[34:37], v3
	v_lshlrev_b32_e32 v2, 4, v104
	s_add_i32 s0, 0, 0x26000
	s_add_i32 s1, 0, 0x26100
	v_add_u32_e32 v3, s0, v2
	v_add_u32_e32 v4, s1, v2
	v_or_b32_e32 v5, 64, v2
	v_or_b32_e32 v7, 0x80, v2
	v_or_b32_e32 v2, 0xc0, v2
	v_add_u32_e32 v6, s0, v5
	v_add_u32_e32 v5, s1, v5
	v_add_u32_e32 v8, s0, v7
	v_add_u32_e32 v7, s1, v7
	v_add_u32_e32 v18, s0, v2
	v_add_u32_e32 v2, s1, v2
	ds_read_b128 v[30:33], v3
	ds_read_b128 v[14:17], v4
	ds_read_b128 v[26:29], v6
	ds_read_b128 v[10:13], v5
	ds_read_b128 v[22:25], v8
	ds_read_b128 v[6:9], v7
	ds_read_b128 v[18:21], v18
	ds_read_b128 v[2:5], v2
	s_waitcnt lgkmcnt(0)
	v_lshl_add_u64 v[66:67], s[36:37], 0, v[66:67]
	s_mov_b64 s[0:1], 0
	s_movk_i32 s6, 0x70
	s_mov_b64 s[4:5], 0x2000
	s_movk_i32 s7, 0x5ff
	v_mov_b32_e32 v69, 0
	s_barrier
	v_add_u32_e32 v79, s33, v70
	v_bitop3_b32 v68, v70, s6, v1 bitop3:0x48
	v_readfirstlane_b32 s8, v79
	v_lshl_add_u64 v[80:81], v[66:67], 0, v[68:69]
	s_mov_b32 m0, s8
	v_add_u32_e32 v68, 0x200, v1
	global_load_lds_dwordx4 v[80:81], off
	v_cmp_lt_u32_e32 vcc, s7, v1
	v_add_u32_e32 v70, 0x2000, v70
	v_lshl_add_u64 v[66:67], v[66:67], 0, s[4:5]
	s_or_b64 s[0:1], vcc, s[0:1]
	v_mov_b32_e32 v1, v68
	v_add_u32_e32 v79, s33, v70
	v_bitop3_b32 v68, v70, s6, v1 bitop3:0x48
	v_readfirstlane_b32 s8, v79
	v_lshl_add_u64 v[80:81], v[66:67], 0, v[68:69]
	s_mov_b32 m0, s8
	v_add_u32_e32 v68, 0x200, v1
	global_load_lds_dwordx4 v[80:81], off
	v_cmp_lt_u32_e32 vcc, s7, v1
	v_add_u32_e32 v70, 0x2000, v70
	v_lshl_add_u64 v[66:67], v[66:67], 0, s[4:5]
	s_or_b64 s[0:1], vcc, s[0:1]
	v_mov_b32_e32 v1, v68
	v_add_u32_e32 v79, s33, v70
	v_bitop3_b32 v68, v70, s6, v1 bitop3:0x48
	v_readfirstlane_b32 s8, v79
	v_lshl_add_u64 v[80:81], v[66:67], 0, v[68:69]
	s_mov_b32 m0, s8
	v_add_u32_e32 v68, 0x200, v1
	global_load_lds_dwordx4 v[80:81], off
	v_cmp_lt_u32_e32 vcc, s7, v1
	v_add_u32_e32 v70, 0x2000, v70
	v_lshl_add_u64 v[66:67], v[66:67], 0, s[4:5]
	s_or_b64 s[0:1], vcc, s[0:1]
	v_mov_b32_e32 v1, v68
	v_add_u32_e32 v79, s33, v70
	v_bitop3_b32 v68, v70, s6, v1 bitop3:0x48
	v_readfirstlane_b32 s8, v79
	v_lshl_add_u64 v[80:81], v[66:67], 0, v[68:69]
	s_mov_b32 m0, s8
	v_add_u32_e32 v68, 0x200, v1
	global_load_lds_dwordx4 v[80:81], off
	v_cmp_lt_u32_e32 vcc, s7, v1
	v_add_u32_e32 v70, 0x2000, v70
	v_lshl_add_u64 v[66:67], v[66:67], 0, s[4:5]
	s_or_b64 s[0:1], vcc, s[0:1]
	v_mov_b32_e32 v1, v68
	s_or_b64 exec, exec, s[0:1]
	v_readfirstlane_b32 s44, v0
	s_nop 3
	s_cmp_lt_u32 s44, 0x100
	s_cbranch_scc0 .Lat_dh1
	v_lshl_add_u32 v1, v103, 9, 0
	v_add_u32_e32 v114, v1, v78
	v_add_u32_e32 v117, v1, v77
	v_add_u32_e32 v115, v1, v76
	v_add_u32_e32 v113, v1, v75
	v_add_u32_e32 v119, v1, v74
	v_add_u32_e32 v118, v1, v72
	v_add_u32_e32 v116, v1, v73
	v_add_u32_e32 v1, v1, v71
	s_mov_b32 s38, 0x5040100
	s_add_u32 s36, s30, s34
	s_addc_u32 s37, s31, s35
	s_add_i32 s30, 0, 0x20000
	v_lshlrev_b32_e32 v112, 7, v103
	s_add_i32 s34, 0, 0x22000
	ds_read_b128 v[156:159], v114
	ds_read_b128 v[160:163], v117
	ds_read_b128 v[164:167], v115
	ds_read_b128 v[168:171], v113
	ds_read_b128 v[172:175], v119
	ds_read_b128 v[176:179], v118
	ds_read_b128 v[180:183], v116
	ds_read_b128 v[184:187], v1
	ds_read_b128 v[188:191], v114 offset:8192
	ds_read_b128 v[192:195], v117 offset:8192
	ds_read_b128 v[196:199], v115 offset:8192
	ds_read_b128 v[200:203], v113 offset:8192
	ds_read_b128 v[204:207], v119 offset:8192
	ds_read_b128 v[208:211], v118 offset:8192
	ds_read_b128 v[212:215], v116 offset:8192
	ds_read_b128 v[216:219], v1 offset:8192
	s_waitcnt lgkmcnt(8)
	v_mfma_f32_16x16x32_bf16 v[66:69], v[156:159], v[62:65], 0
	v_mfma_f32_16x16x32_bf16 v[66:69], v[160:163], v[58:61], v[66:69]
	v_mfma_f32_16x16x32_bf16 v[66:69], v[164:167], v[54:57], v[66:69]
	v_mfma_f32_16x16x32_bf16 v[66:69], v[168:171], v[50:53], v[66:69]
	v_mfma_f32_16x16x32_bf16 v[66:69], v[172:175], v[46:49], v[66:69]
	v_mfma_f32_16x16x32_bf16 v[66:69], v[176:179], v[42:45], v[66:69]
	v_mfma_f32_16x16x32_bf16 v[66:69], v[180:183], v[38:41], v[66:69]
	v_mfma_f32_16x16x32_bf16 v[66:69], v[184:187], v[34:37], v[66:69]
	s_waitcnt lgkmcnt(0)
	v_mfma_f32_16x16x32_bf16 v[70:73], v[188:191], v[62:65], 0
	v_mfma_f32_16x16x32_bf16 v[70:73], v[192:195], v[58:61], v[70:73]
	v_mfma_f32_16x16x32_bf16 v[70:73], v[196:199], v[54:57], v[70:73]
	v_mfma_f32_16x16x32_bf16 v[70:73], v[200:203], v[50:53], v[70:73]
	v_mfma_f32_16x16x32_bf16 v[70:73], v[204:207], v[46:49], v[70:73]
	v_mfma_f32_16x16x32_bf16 v[70:73], v[208:211], v[42:45], v[70:73]
	v_mfma_f32_16x16x32_bf16 v[70:73], v[212:215], v[38:41], v[70:73]
	v_mfma_f32_16x16x32_bf16 v[70:73], v[216:219], v[34:37], v[70:73]
	ds_read_b128 v[156:159], v114 offset:16384
	ds_read_b128 v[160:163], v117 offset:16384
	ds_read_b128 v[164:167], v115 offset:16384
	ds_read_b128 v[168:171], v113 offset:16384
	ds_read_b128 v[172:175], v119 offset:16384
	ds_read_b128 v[176:179], v118 offset:16384
	ds_read_b128 v[180:183], v116 offset:16384
	ds_read_b128 v[184:187], v1 offset:16384
	ds_read_b128 v[188:191], v114 offset:24576
	ds_read_b128 v[192:195], v117 offset:24576
	ds_read_b128 v[196:199], v115 offset:24576
	ds_read_b128 v[200:203], v113 offset:24576
	ds_read_b128 v[204:207], v119 offset:24576
	ds_read_b128 v[208:211], v118 offset:24576
	ds_read_b128 v[212:215], v116 offset:24576
	ds_read_b128 v[216:219], v1 offset:24576
	s_waitcnt lgkmcnt(8)
	v_mfma_f32_16x16x32_bf16 v[74:77], v[156:159], v[62:65], 0
	v_mfma_f32_16x16x32_bf16 v[74:77], v[160:163], v[58:61], v[74:77]
	v_mfma_f32_16x16x32_bf16 v[74:77], v[164:167], v[54:57], v[74:77]
	v_mfma_f32_16x16x32_bf16 v[74:77], v[168:171], v[50:53], v[74:77]
	v_mfma_f32_16x16x32_bf16 v[74:77], v[172:175], v[46:49], v[74:77]
	v_mfma_f32_16x16x32_bf16 v[74:77], v[176:179], v[42:45], v[74:77]
	v_mfma_f32_16x16x32_bf16 v[74:77], v[180:183], v[38:41], v[74:77]
	v_mfma_f32_16x16x32_bf16 v[74:77], v[184:187], v[34:37], v[74:77]
	s_waitcnt lgkmcnt(0)
	v_mfma_f32_16x16x32_bf16 v[220:223], v[188:191], v[62:65], 0
	v_mfma_f32_16x16x32_bf16 v[220:223], v[192:195], v[58:61], v[220:223]
	v_mfma_f32_16x16x32_bf16 v[220:223], v[196:199], v[54:57], v[220:223]
	v_mfma_f32_16x16x32_bf16 v[220:223], v[200:203], v[50:53], v[220:223]
	v_mfma_f32_16x16x32_bf16 v[220:223], v[204:207], v[46:49], v[220:223]
	v_mfma_f32_16x16x32_bf16 v[220:223], v[208:211], v[42:45], v[220:223]
	v_mfma_f32_16x16x32_bf16 v[220:223], v[212:215], v[38:41], v[220:223]
	v_mfma_f32_16x16x32_bf16 v[220:223], v[216:219], v[34:37], v[220:223]
	s_nop 7
	v_cvt_pk_bf16_f32 v70, v70, s0
	v_cvt_pk_bf16_f32 v71, v71, s0
	v_cvt_pk_bf16_f32 v72, v72, s0
	v_cvt_pk_bf16_f32 v73, v73, s0
	v_cvt_pk_bf16_f32 v82, v66, s0
	v_cvt_pk_bf16_f32 v83, v67, s0
	v_cvt_pk_bf16_f32 v84, v68, s0
	v_cvt_pk_bf16_f32 v85, v69, s0
	v_lshlrev_b32_e32 v106, 2, v104
	v_cmp_gt_u32_e32 vcc, v106, v102
	v_cvt_pk_bf16_f32 v78, v74, s0
	v_or_b32_e32 v74, 3, v106
	v_cvt_pk_bf16_f32 v79, v75, s0
	s_nop 1
	v_mov_b32_e32 v66, v220
	v_mov_b32_e32 v67, v221
	v_mov_b32_e32 v68, v222
	v_mov_b32_e32 v69, v223
	v_cvt_pk_bf16_f32 v80, v76, s0
	v_cvt_pk_bf16_f32 v81, v77, s0
	v_cmp_gt_u32_e64 s[6:7], v74, v102
	v_cndmask_b32_e64 v75, v82, 0, vcc
	v_or_b32_e32 v120, 51, v106
	s_nop 2
	v_cvt_pk_bf16_f32 v89, v69, s0
	v_or_b32_e32 v69, 2, v106
	v_cvt_pk_bf16_f32 v66, v66, s0
	v_cvt_pk_bf16_f32 v67, v67, s0
	v_cvt_pk_bf16_f32 v68, v68, s0
	v_cmp_lt_u32_e64 s[0:1], v106, v102
	v_cmp_gt_u32_e64 s[4:5], v69, v102
	v_cndmask_b32_e64 v77, v85, 0, s[6:7]
	v_cndmask_b32_e64 v76, 0, v83, s[0:1]
	v_cndmask_b32_e64 v69, v84, 0, s[4:5]
	v_perm_b32 v74, v76, v75, s38
	v_perm_b32 v75, v77, v69, s38
	v_or_b32_e32 v69, 17, v106
	v_or_b32_e32 v76, 16, v106
	v_cmp_gt_u32_e64 s[8:9], v76, v102
	v_cmp_gt_u32_e64 s[10:11], v69, v102
	s_nop 0
	v_cndmask_b32_e64 v70, v70, 0, s[8:9]
	v_cndmask_b32_e64 v69, v71, 0, s[10:11]
	v_perm_b32 v76, v69, v70, s38
	v_or_b32_e32 v69, 19, v106
	v_or_b32_e32 v70, 18, v106
	v_cmp_gt_u32_e64 s[16:17], v70, v102
	v_cmp_gt_u32_e64 s[20:21], v69, v102
	v_or_b32_e32 v71, 35, v106
	v_cndmask_b32_e64 v70, v72, 0, s[16:17]
	v_cndmask_b32_e64 v69, v73, 0, s[20:21]
	v_perm_b32 v77, v69, v70, s38
	v_or_b32_e32 v69, 33, v106
	v_or_b32_e32 v70, 34, v106
	v_or_b32_e32 v72, 32, v106
	v_cmp_gt_u32_e64 s[12:13], v72, v102
	v_cmp_gt_u32_e64 s[14:15], v69, v102
	v_cmp_gt_u32_e64 s[18:19], v70, v102
	v_cmp_gt_u32_e64 s[22:23], v71, v102
	v_cndmask_b32_e64 v72, v78, 0, s[12:13]
	v_cndmask_b32_e64 v69, v79, 0, s[14:15]
	v_cndmask_b32_e64 v70, v80, 0, s[18:19]
	v_cndmask_b32_e64 v71, v81, 0, s[22:23]
	v_perm_b32 v86, v69, v72, s38
	v_perm_b32 v87, v71, v70, s38
	v_or_b32_e32 v69, 49, v106
	v_or_b32_e32 v70, 48, v106
	v_cmp_gt_u32_e64 s[24:25], v70, v102
	v_cmp_gt_u32_e64 s[26:27], v69, v102
	s_nop 0
	v_cndmask_b32_e64 v66, v66, 0, s[24:25]
	v_cndmask_b32_e64 v67, v67, 0, s[26:27]
	v_perm_b32 v88, v67, v66, s38
	v_or_b32_e32 v66, 50, v106
	v_cmp_gt_u32_e64 s[28:29], v66, v102
	v_lshrrev_b32_e32 v67, 1, v104
	v_bfe_u32 v66, v0, 1, 3
	v_cndmask_b32_e64 v121, v68, 0, s[28:29]
	v_lshrrev_b32_e32 v68, 1, v0
	v_bitop3_b32 v69, v67, v68, 7 bitop3:0x78
	v_and_b32_e32 v111, 8, v68
	v_lshlrev_b32_e32 v109, 4, v69
	v_add3_u32 v70, s30, v111, v112
	v_add_u32_e32 v128, v70, v109
	ds_read2st64_b64 v[90:93], v128 offset1:4
	v_bitop3_b32 v68, v67, v66, 2 bitop3:0x36
	v_lshlrev_b32_e32 v110, 4, v68
	v_bitop3_b32 v71, v67, v66, 4 bitop3:0x36
	v_bitop3_b32 v72, v67, v66, 6 bitop3:0x36
	s_waitcnt lgkmcnt(0)
	v_mov_b32_e32 v82, v90
	v_add_u32_e32 v90, v70, v110
	ds_read2st64_b64 v[66:69], v90 offset1:4
	v_lshlrev_b32_e32 v107, 4, v71
	v_lshlrev_b32_e32 v108, 4, v72
	v_add_u32_e32 v136, v70, v107
	v_add_u32_e32 v140, v70, v108
	ds_read2st64_b64 v[94:97], v136 offset1:4
	ds_read2st64_b64 v[70:73], v140 offset1:4
	v_mov_b32_e32 v83, v91
	s_waitcnt lgkmcnt(0)
	v_mov_b32_e32 v84, v66
	v_mov_b32_e32 v85, v67
	v_mov_b32_e32 v78, v94
	v_mov_b32_e32 v79, v95
	v_mov_b32_e32 v80, v70
	v_mov_b32_e32 v81, v71
	v_mfma_f32_16x16x32_bf16 v[98:101], v[82:85], v[74:77], 0
	v_cmp_gt_u32_e64 s[30:31], v120, v102
	v_mov_b32_e32 v67, v93
	v_mov_b32_e32 v70, v96
	v_cndmask_b32_e64 v66, v89, 0, s[30:31]
	v_perm_b32 v89, v66, v121, s38
	v_mov_b32_e32 v66, v92
	ds_read_b128 v[120:123], v114 offset:32768
	ds_read_b128 v[124:127], v114 offset:40960
	v_mfma_f32_16x16x32_bf16 v[98:101], v[78:81], v[86:89], v[98:101]
	v_mov_b32_e32 v71, v97
	ds_read2st64_b64 v[128:131], v128 offset0:8 offset1:12
	ds_read2st64_b64 v[90:93], v90 offset0:8 offset1:12
	ds_read2st64_b64 v[136:139], v136 offset0:8 offset1:12
	s_waitcnt lgkmcnt(0)
	v_mfma_f32_16x16x32_bf16 v[120:123], v[120:123], v[62:65], v[98:101]
	v_mov_b32_e32 v94, v128
	v_mov_b32_e32 v95, v129
	v_mfma_f32_16x16x32_bf16 v[98:101], v[66:69], v[74:77], 0
	v_mov_b32_e32 v96, v90
	v_mov_b32_e32 v97, v91
	v_mov_b32_e32 v90, v130
	v_mfma_f32_16x16x32_bf16 v[132:135], v[70:73], v[86:89], v[98:101]
	v_mov_b32_e32 v91, v131
	s_nop 2
	ds_read2st64_b64 v[98:101], v140 offset0:8 offset1:12
	v_mfma_f32_16x16x32_bf16 v[124:127], v[124:127], v[62:65], v[132:135]
	ds_read_b128 v[144:147], v114 offset:49152
	ds_read_b128 v[148:151], v114 offset:57344
	ds_read_b128 v[128:131], v115 offset:32768
	v_mov_b32_e32 v132, v136
	v_mov_b32_e32 v133, v137
	s_waitcnt lgkmcnt(0)
	v_mov_b32_e32 v134, v98
	v_mov_b32_e32 v135, v99
	v_mov_b32_e32 v98, v138
	v_mov_b32_e32 v99, v139
	v_mfma_f32_16x16x32_bf16 v[140:143], v[94:97], v[74:77], 0
	v_mfma_f32_16x16x32_bf16 v[74:77], v[90:93], v[74:77], 0
	v_mfma_f32_16x16x32_bf16 v[140:143], v[132:135], v[86:89], v[140:143]
	v_mfma_f32_16x16x32_bf16 v[74:77], v[98:101], v[86:89], v[74:77]
	ds_read_b128 v[86:89], v117 offset:32768
	v_mfma_f32_16x16x32_bf16 v[140:143], v[144:147], v[62:65], v[140:143]
	v_mfma_f32_16x16x32_bf16 v[62:65], v[148:151], v[62:65], v[74:77]
	s_nop 4
	ds_read_b128 v[74:77], v117 offset:40960
	s_waitcnt lgkmcnt(0)
	v_mfma_f32_16x16x32_bf16 v[86:89], v[86:89], v[58:61], v[120:123]
	s_nop 2
	ds_read_b128 v[120:123], v117 offset:49152
	v_mfma_f32_16x16x32_bf16 v[74:77], v[74:77], v[58:61], v[124:127]
	s_nop 2
	ds_read_b128 v[124:127], v117 offset:57344
	s_waitcnt lgkmcnt(0)
	v_mfma_f32_16x16x32_bf16 v[120:123], v[120:123], v[58:61], v[140:143]
	v_mfma_f32_16x16x32_bf16 v[58:61], v[124:127], v[58:61], v[62:65]
	ds_read_b128 v[124:127], v115 offset:49152
	s_nop 1
	ds_read_b128 v[62:65], v115 offset:40960
	s_waitcnt lgkmcnt(0)
	v_mfma_f32_16x16x32_bf16 v[62:65], v[62:65], v[54:57], v[74:77]
	s_nop 2
	ds_read_b128 v[74:77], v115 offset:57344
	v_cndmask_b32_e64 v115, 0, 1.0, s[0:1]
	v_mfma_f32_16x16x32_bf16 v[120:123], v[124:127], v[54:57], v[120:123]
	ds_read_b128 v[124:127], v113 offset:32768
	v_mfma_f32_16x16x32_bf16 v[86:89], v[128:131], v[54:57], v[86:89]
	s_waitcnt lgkmcnt(0)
	v_mfma_f32_16x16x32_bf16 v[54:57], v[74:77], v[54:57], v[58:61]
	s_nop 2
	ds_read_b128 v[58:61], v113 offset:40960
	v_mfma_f32_16x16x32_bf16 v[74:77], v[124:127], v[50:53], v[86:89]
	s_nop 2
	ds_read_b128 v[86:89], v113 offset:49152
	s_waitcnt lgkmcnt(0)
	v_mfma_f32_16x16x32_bf16 v[58:61], v[58:61], v[50:53], v[62:65]
	s_nop 2
	ds_read_b128 v[62:65], v113 offset:57344
	v_mov_b32_e32 v113, 0x3f80
	v_cndmask_b32_e64 v114, v113, 0, vcc
	v_mfma_f32_16x16x32_bf16 v[86:89], v[86:89], v[50:53], v[120:123]
	s_nop 2
	ds_read_b128 v[120:123], v119 offset:32768
	s_waitcnt lgkmcnt(0)
	v_mfma_f32_16x16x32_bf16 v[50:53], v[62:65], v[50:53], v[54:57]
	s_nop 2
	ds_read_b128 v[54:57], v119 offset:40960
	v_mfma_f32_16x16x32_bf16 v[62:65], v[120:123], v[46:49], v[74:77]
	s_nop 2
	ds_read_b128 v[74:77], v119 offset:49152
	s_waitcnt lgkmcnt(0)
	v_mfma_f32_16x16x32_bf16 v[74:77], v[74:77], v[46:49], v[86:89]
	s_nop 2
	ds_read_b128 v[86:89], v118 offset:32768
	v_mfma_f32_16x16x32_bf16 v[54:57], v[54:57], v[46:49], v[58:61]
	s_nop 2
	ds_read_b128 v[58:61], v119 offset:57344
	s_waitcnt lgkmcnt(0)
	v_mfma_f32_16x16x32_bf16 v[46:49], v[58:61], v[46:49], v[50:53]
	s_nop 2
	ds_read_b128 v[50:53], v118 offset:40960
	v_mfma_f32_16x16x32_bf16 v[58:61], v[86:89], v[42:45], v[62:65]
	s_nop 2
	ds_read_b128 v[62:65], v118 offset:49152
	s_waitcnt lgkmcnt(0)
	v_mfma_f32_16x16x32_bf16 v[62:65], v[62:65], v[42:45], v[74:77]
	s_nop 2
	ds_read_b128 v[74:77], v116 offset:32768
	v_mfma_f32_16x16x32_bf16 v[50:53], v[50:53], v[42:45], v[54:57]
	s_nop 2
	ds_read_b128 v[54:57], v118 offset:57344
	s_waitcnt lgkmcnt(0)
	v_mfma_f32_16x16x32_bf16 v[42:45], v[54:57], v[42:45], v[46:49]
	s_nop 2
	ds_read_b128 v[46:49], v116 offset:40960
	ds_read_b128 v[54:57], v116 offset:49152
	ds_read_b128 v[86:89], v116 offset:57344
	v_cndmask_b32_e64 v116, v113, 0, s[4:5]
	v_mfma_f32_16x16x32_bf16 v[58:61], v[74:77], v[38:41], v[58:61]
	s_waitcnt lgkmcnt(0)
	v_mfma_f32_16x16x32_bf16 v[46:49], v[46:49], v[38:41], v[50:53]
	s_nop 2
	ds_read_b128 v[50:53], v1 offset:32768
	ds_read_b128 v[74:77], v1 offset:40960
	v_mfma_f32_16x16x32_bf16 v[54:57], v[54:57], v[38:41], v[62:65]
	v_mfma_f32_16x16x32_bf16 v[38:41], v[86:89], v[38:41], v[42:45]
	v_cndmask_b32_e64 v87, v113, 0, s[12:13]
	s_nop 0
	v_cndmask_b32_e64 v62, 1.0, 0, s[6:7]
	v_cndmask_b32_e64 v63, v113, 0, s[8:9]
	ds_read_b128 v[42:45], v1 offset:49152
	s_waitcnt lgkmcnt(0)
	v_mfma_f32_16x16x32_bf16 v[50:53], v[50:53], v[34:37], v[58:61]
	v_cndmask_b32_e64 v64, 1.0, 0, s[10:11]
	v_cndmask_b32_e64 v65, v113, 0, s[16:17]
	v_cndmask_b32_e64 v86, 1.0, 0, s[20:21]
	ds_read_b128 v[58:61], v1 offset:57344
	v_cndmask_b32_e64 v1, 1.0, 0, s[14:15]
	v_mfma_f32_16x16x32_bf16 v[46:49], v[74:77], v[34:37], v[46:49]
	v_cndmask_b32_e64 v74, v113, 0, s[18:19]
	v_cndmask_b32_e64 v75, 1.0, 0, s[22:23]
	v_cndmask_b32_e64 v76, v113, 0, s[24:25]
	v_mfma_f32_16x16x32_bf16 v[42:45], v[42:45], v[34:37], v[54:57]
	v_cndmask_b32_e64 v77, 1.0, 0, s[26:27]
	v_cndmask_b32_e64 v88, v113, 0, s[28:29]
	v_cndmask_b32_e64 v89, 1.0, 0, s[30:31]
	s_waitcnt lgkmcnt(0)
	v_mfma_f32_16x16x32_bf16 v[38:41], v[58:61], v[34:37], v[38:41]
	v_or_b32_e32 v34, v1, v87
	v_add3_u32 v1, s34, v111, v112
	v_add_u32_e32 v113, v1, v109
	v_add_u32_e32 v118, v1, v110
	v_or_b32_e32 v55, v62, v116
	v_or_b32_e32 v56, v64, v63
	v_or_b32_e32 v57, v86, v65
	v_or_b32_e32 v35, v75, v74
	ds_read2st64_b64 v[62:65], v113 offset1:4
	v_or_b32_e32 v36, v77, v76
	ds_read2st64_b64 v[74:77], v118 offset1:4
	v_add_u32_e32 v119, v1, v107
	v_add_u32_e32 v1, v1, v108
	v_or_b32_e32 v54, v115, v114
	v_or_b32_e32 v37, v89, v88
	ds_read2st64_b64 v[86:89], v119 offset1:4
	ds_read2st64_b64 v[114:117], v1 offset1:4
	v_mfma_f32_16x16x32_bf16 v[58:61], v[82:85], v[54:57], 0
	s_waitcnt lgkmcnt(0)
	v_mov_b32_e32 v82, v62
	v_mov_b32_e32 v83, v63
	v_mov_b32_e32 v84, v74
	v_mov_b32_e32 v85, v75
	v_mfma_f32_16x16x32_bf16 v[66:69], v[66:69], v[54:57], 0
	v_mov_b32_e32 v74, v64
	v_mov_b32_e32 v75, v65
	ds_read2st64_b64 v[62:65], v113 offset0:8 offset1:12
	v_mfma_f32_16x16x32_bf16 v[58:61], v[78:81], v[34:37], v[58:61]
	v_mov_b32_e32 v78, v86
	v_mov_b32_e32 v79, v87
	v_mov_b32_e32 v80, v114
	v_mov_b32_e32 v81, v115
	v_mfma_f32_16x16x32_bf16 v[82:85], v[82:85], v[54:57], 0
	v_mov_b32_e32 v114, v88
	v_mov_b32_e32 v115, v89
	v_mul_f32_e32 v51, 0x3d800000, v51
	v_mfma_f32_16x16x32_bf16 v[66:69], v[70:73], v[34:37], v[66:69]
	v_mul_f32_e32 v52, 0x3d800000, v52
	v_mul_f32_e32 v53, 0x3d800000, v53
	s_mov_b32 s34, 0xff61b1e6
	v_mfma_f32_16x16x32_bf16 v[70:73], v[94:97], v[54:57], 0
	v_mul_f32_e32 v46, 0x3d800000, v46
	s_nop 2
	v_add_f32_e32 v86, v66, v26
	v_add_f32_e32 v87, v67, v27
	v_mfma_f32_16x16x32_bf16 v[78:81], v[78:81], v[34:37], v[82:85]
	v_add_f32_e32 v94, v68, v28
	v_add_f32_e32 v95, v69, v29
	ds_read2st64_b64 v[66:69], v119 offset0:8 offset1:12
	v_add_f32_e32 v82, v58, v30
	v_add_f32_e32 v83, v59, v31
	v_add_f32_e32 v84, v60, v32
	v_add_f32_e32 v85, v61, v33
	v_mfma_f32_16x16x32_bf16 v[30:33], v[132:135], v[34:37], v[70:73]
	v_mul_f32_e32 v47, 0x3d800000, v47
	v_mul_f32_e32 v48, 0x3d800000, v48
	v_mul_f32_e32 v49, 0x3d800000, v49
	v_mfma_f32_16x16x32_bf16 v[26:29], v[90:93], v[54:57], 0
	ds_read2st64_b64 v[70:73], v1 offset0:8 offset1:12
	s_nop 2
	v_add_f32_e32 v90, v30, v22
	v_add_f32_e32 v91, v31, v23
	v_add_f32_e32 v92, v32, v24
	v_add_f32_e32 v88, v33, v25
	ds_read2st64_b64 v[22:25], v118 offset0:8 offset1:12
	v_mfma_f32_16x16x32_bf16 v[58:61], v[74:77], v[54:57], 0
	s_waitcnt lgkmcnt(0)
	v_mov_b32_e32 v74, v66
	v_mov_b32_e32 v75, v67
	v_mov_b32_e32 v76, v70
	v_mfma_f32_16x16x32_bf16 v[30:33], v[114:117], v[34:37], v[58:61]
	v_mov_b32_e32 v77, v71
	v_mov_b32_e32 v70, v68
	v_add_f32_e32 v68, v79, v15
	v_mov_b32_e32 v58, v62
	v_mov_b32_e32 v59, v63
	v_mov_b32_e32 v60, v22
	v_mov_b32_e32 v61, v23
	v_mfma_f32_16x16x32_bf16 v[26:29], v[98:101], v[34:37], v[26:29]
	v_rcp_f32_e32 v62, v85
	v_rcp_f32_e32 v63, v86
	v_rcp_f32_e32 v79, v87
	v_mfma_f32_16x16x32_bf16 v[58:61], v[58:61], v[54:57], 0
	v_mov_b32_e32 v71, v69
	s_nop 2
	v_add_f32_e32 v26, v26, v18
	v_add_f32_e32 v1, v27, v19
	v_add_f32_e32 v27, v28, v20
	v_add_f32_e32 v28, v29, v21
	v_mfma_f32_16x16x32_bf16 v[18:21], v[74:77], v[34:37], v[58:61]
	v_mul_f32_e32 v29, 0x3d800000, v50
	v_rcp_f32_e32 v50, v82
	v_add_f32_e32 v69, v80, v16
	v_rcp_f32_e32 v60, v83
	v_rcp_f32_e32 v61, v84
	v_add_f32_e32 v74, v81, v17
	v_rcp_f32_e32 v80, v94
	v_rcp_f32_e32 v81, v95
	v_add_f32_e32 v75, v30, v10
	v_add_f32_e32 v76, v31, v11
	v_mul_f32_e32 v30, 0x3d800000, v42
	v_mul_f32_e32 v31, 0x3d800000, v43
	v_add_f32_e32 v42, v18, v6
	v_add_f32_e32 v43, v19, v7
	v_mul_f32_e32 v18, v29, v50
	v_mul_f32_e32 v19, v51, v60
	v_rcp_f32_e32 v82, v90
	v_rcp_f32_e32 v83, v91
	v_add_f32_e32 v77, v32, v12
	v_mul_f32_e32 v32, 0x3d800000, v44
	v_add_f32_e32 v44, v20, v8
	v_max3_f32 v18, v18, s34, v19
	v_mul_f32_e32 v19, v52, v61
	v_mul_f32_e32 v20, v53, v62
	v_rcp_f32_e32 v84, v92
	v_rcp_f32_e32 v85, v88
	v_max3_f32 v18, v18, v19, v20
	v_mul_f32_e32 v19, v46, v63
	v_mul_f32_e32 v20, v47, v79
	v_rcp_f32_e32 v86, v26
	v_rcp_f32_e32 v87, v1
	v_max3_f32 v18, v18, v19, v20
	v_mul_f32_e32 v19, v48, v80
	v_mul_f32_e32 v20, v49, v81
	v_rcp_f32_e32 v88, v27
	v_rcp_f32_e32 v89, v28
	v_add_f32_e32 v67, v78, v14
	v_add_f32_e32 v78, v33, v13
	v_mul_f32_e32 v33, 0x3d800000, v45
	v_max3_f32 v18, v18, v19, v20
	v_mul_f32_e32 v19, v30, v82
	v_mul_f32_e32 v20, v31, v83
	v_max3_f32 v18, v18, v19, v20
	v_mul_f32_e32 v19, v32, v84
	v_mul_f32_e32 v20, v33, v85
	v_mul_f32_e32 v38, 0x3d800000, v38
	v_mul_f32_e32 v39, 0x3d800000, v39
	v_max3_f32 v18, v18, v19, v20
	v_mul_f32_e32 v1, v38, v86
	v_mul_f32_e32 v19, v39, v87
	v_mul_f32_e32 v40, 0x3d800000, v40
	v_mul_f32_e32 v41, 0x3d800000, v41
	v_max3_f32 v1, v18, v1, v19
	v_mul_f32_e32 v18, v40, v88
	v_mul_f32_e32 v19, v41, v89
	v_max3_f32 v1, v1, v18, v19
	v_mbcnt_lo_u32_b32 v18, -1, 0
	v_mbcnt_hi_u32_b32 v26, -1, v18
	v_and_b32_e32 v19, 64, v26
	v_xor_b32_e32 v18, 16, v26
	v_add_u32_e32 v27, 64, v19
	v_cmp_lt_i32_e64 s[34:35], v18, v27
	v_mov_b32_e32 v22, v64
	v_mov_b32_e32 v23, v65
	v_cndmask_b32_e64 v18, v26, v18, s[34:35]
	v_lshlrev_b32_e32 v64, 2, v18
	ds_bpermute_b32 v28, v64, v1
	v_add_f32_e32 v45, v21, v9
	v_mfma_f32_16x16x32_bf16 v[18:21], v[22:25], v[54:57], 0
	v_lshlrev_b32_e32 v58, 9, v102
	v_mov_b32_e32 v59, 0
	s_waitcnt lgkmcnt(0)
	v_max_f32_e32 v24, v28, v28
	v_max_f32_e32 v24, v1, v24
	v_xor_b32_e32 v1, 32, v26
	v_cmp_lt_i32_e64 s[34:35], v1, v27
	v_lshl_add_u64 v[22:23], s[36:37], 0, v[58:59]
	v_lshlrev_b32_e32 v58, 3, v104
	v_cndmask_b32_e64 v1, v26, v1, s[34:35]
	v_lshlrev_b32_e32 v65, 2, v1
	ds_bpermute_b32 v25, v65, v24
	v_lshl_add_u64 v[22:23], v[22:23], 0, v[58:59]
	v_and_b32_e32 v58, 0x100, v0
	v_lshrrev_b32_e32 v66, 8, v0
	v_lshl_add_u64 v[0:1], v[22:23], 0, v[58:59]
	s_waitcnt lgkmcnt(0)
	v_max_f32_e32 v22, v25, v25
	v_max_f32_e32 v54, v24, v22
	v_fma_f32 v22, v29, v50, -v54
	v_mul_f32_e32 v22, 0x3fb8aa3b, v22
	v_fma_f32 v23, v51, v60, -v54
	v_exp_f32_e32 v22, v22
	v_mul_f32_e32 v23, 0x3fb8aa3b, v23
	v_fma_f32 v24, v52, v61, -v54
	v_exp_f32_e32 v23, v23
	v_mul_f32_e32 v24, 0x3fb8aa3b, v24
	v_fma_f32 v25, v53, v62, -v54
	v_exp_f32_e32 v24, v24
	v_mul_f32_e32 v25, 0x3fb8aa3b, v25
	v_fma_f32 v26, v46, v63, -v54
	v_exp_f32_e32 v25, v25
	v_mul_f32_e32 v26, 0x3fb8aa3b, v26
	v_fma_f32 v27, v47, v79, -v54
	v_exp_f32_e32 v26, v26
	v_mul_f32_e32 v27, 0x3fb8aa3b, v27
	v_fma_f32 v28, v48, v80, -v54
	v_add_f32_e32 v46, 0, v22
	v_exp_f32_e32 v27, v27
	v_mul_f32_e32 v28, 0x3fb8aa3b, v28
	v_fma_f32 v29, v49, v81, -v54
	v_add_f32_e32 v46, v46, v23
	v_exp_f32_e32 v28, v28
	v_mul_f32_e32 v29, 0x3fb8aa3b, v29
	v_add_f32_e32 v46, v46, v24
	v_fma_f32 v30, v30, v82, -v54
	v_exp_f32_e32 v29, v29
	v_add_f32_e32 v46, v46, v25
	v_mul_f32_e32 v30, 0x3fb8aa3b, v30
	v_fma_f32 v31, v31, v83, -v54
	v_add_f32_e32 v46, v46, v26
	v_exp_f32_e32 v30, v30
	v_mul_f32_e32 v31, 0x3fb8aa3b, v31
	v_fma_f32 v32, v32, v84, -v54
	v_add_f32_e32 v46, v46, v27
	v_exp_f32_e32 v31, v31
	v_mul_f32_e32 v32, 0x3fb8aa3b, v32
	v_fma_f32 v33, v33, v85, -v54
	v_add_f32_e32 v46, v46, v28
	v_exp_f32_e32 v32, v32
	v_mul_f32_e32 v33, 0x3fb8aa3b, v33
	v_fma_f32 v38, v38, v86, -v54
	v_add_f32_e32 v46, v46, v29
	v_exp_f32_e32 v33, v33
	v_mul_f32_e32 v38, 0x3fb8aa3b, v38
	v_fma_f32 v39, v39, v87, -v54
	v_add_f32_e32 v46, v46, v30
	v_exp_f32_e32 v38, v38
	v_mul_f32_e32 v39, 0x3fb8aa3b, v39
	v_fma_f32 v40, v40, v88, -v54
	v_add_f32_e32 v46, v46, v31
	v_exp_f32_e32 v39, v39
	v_mul_f32_e32 v40, 0x3fb8aa3b, v40
	v_fma_f32 v41, v41, v89, -v54
	v_add_f32_e32 v46, v46, v32
	v_exp_f32_e32 v40, v40
	v_mul_f32_e32 v41, 0x3fb8aa3b, v41
	v_add_f32_e32 v46, v46, v33
	v_exp_f32_e32 v41, v41
	v_add_f32_e32 v46, v46, v38
	v_add_f32_e32 v46, v46, v39
	v_add_f32_e32 v46, v46, v40
	v_add_f32_e32 v58, v46, v41
	ds_bpermute_b32 v79, v64, v58
	global_load_dwordx2 v[62:63], v[0:1], off
	global_load_dwordx2 v[60:61], v[0:1], off offset:32
	global_load_dwordx2 v[56:57], v[0:1], off offset:64
	global_load_dwordx2 v[52:53], v[0:1], off offset:96
	global_load_dwordx2 v[54:55], v[0:1], off offset:128
	global_load_dwordx2 v[50:51], v[0:1], off offset:160
	global_load_dwordx2 v[48:49], v[0:1], off offset:192
	global_load_dwordx2 v[46:47], v[0:1], off offset:224
	v_mfma_f32_16x16x32_bf16 v[18:21], v[70:73], v[34:37], v[18:21]
	v_rcp_f32_e32 v34, v75
	s_waitcnt lgkmcnt(0)
	v_add_f32_e32 v0, v58, v79
	ds_bpermute_b32 v1, v65, v0
	v_rcp_f32_e32 v35, v76
	v_rcp_f32_e32 v36, v77
	s_nop 1
	v_add_f32_e32 v58, v18, v2
	v_rcp_f32_e32 v18, v67
	s_waitcnt lgkmcnt(0)
	v_add_f32_e32 v0, v0, v1
	v_rcp_f32_e32 v0, v0
	v_add_f32_e32 v1, v19, v3
	v_rcp_f32_e32 v19, v68
	v_add_f32_e32 v70, v20, v4
	v_add_f32_e32 v71, v21, v5
	v_rcp_f32_e32 v20, v69
	v_rcp_f32_e32 v21, v74
	v_mul_f32_e32 v0, 0x43800000, v0
	v_pk_mul_f32 v[22:23], v[0:1], v[22:23] op_sel_hi:[0,1]
	v_pk_mul_f32 v[18:19], v[22:23], v[18:19]
	v_pk_mul_f32 v[22:23], v[0:1], v[24:25] op_sel_hi:[0,1]
	v_pk_mul_f32 v[20:21], v[22:23], v[20:21]
	v_rcp_f32_e32 v37, v78
	v_pk_mul_f32 v[14:15], v[14:15], v[18:19]
	v_pk_mul_f32 v[16:17], v[16:17], v[20:21]
	v_cvt_pk_f16_f32 v14, v14, v15
	v_cvt_pk_f16_f32 v15, v16, v17
	v_pk_mul_f32 v[16:17], v[0:1], v[26:27] op_sel_hi:[0,1]
	v_pk_mul_f32 v[16:17], v[16:17], v[34:35]
	v_cvt_pk_bf16_f32 v18, v18, v19
	v_cvt_pk_bf16_f32 v19, v20, v21
	v_pk_mul_f32 v[10:11], v[10:11], v[16:17]
	v_cvt_pk_bf16_f32 v20, v16, v17
	v_pk_mul_f32 v[16:17], v[0:1], v[28:29] op_sel_hi:[0,1]
	v_pk_mul_f32 v[72:73], v[16:17], v[36:37]
	v_rcp_f32_e32 v16, v42
	v_rcp_f32_e32 v17, v43
	v_rcp_f32_e32 v24, v44
	v_rcp_f32_e32 v25, v45
	v_rcp_f32_e32 v26, v58
	v_rcp_f32_e32 v27, v1
	v_pk_mul_f32 v[22:23], v[0:1], v[30:31] op_sel_hi:[0,1]
	v_pk_mul_f32 v[76:77], v[22:23], v[16:17]
	v_pk_mul_f32 v[16:17], v[0:1], v[32:33] op_sel_hi:[0,1]
	v_pk_mul_f32 v[78:79], v[16:17], v[24:25]
	v_pk_mul_f32 v[16:17], v[0:1], v[38:39] op_sel_hi:[0,1]
	s_add_i32 s34, 0, 0x24000
	v_pk_mul_f32 v[80:81], v[16:17], v[26:27]
	v_add3_u32 v16, s34, v112, v111
	v_add_u32_e32 v17, v16, v109
	v_add_u32_e32 v58, v16, v110
	s_barrier
	ds_write_b128 v152, v[70:73]
	ds_write_b128 v152, v[76:79] offset:1024
	ds_write_b64 v153, v[0:1] offset:2048
	ds_write_b64 v153, v[10:11] offset:2560
	ds_write_b64 v153, v[14:15] offset:3072
	ds_write_b64 v153, v[18:19] offset:3584
	ds_write_b64 v153, v[40:41] offset:4096
	ds_write_b64 v153, v[80:81] offset:4608
	ds_write_b32 v154, v20 offset:5120
	s_waitcnt lgkmcnt(0)
	s_branch .Lat_join
